# speedup vs baseline: 1.0723x; 1.0204x over previous
.LBB1_77:
	s_add_i32 s71, s40, 0
	global_load_dword v6, v[168:169], off sc1
	global_load_dword v7, v[168:169], off sc1
	v_add_u32_e32 v249, v61, v207
	ds_read_b128 v[64:67], v249
	ds_read_b128 v[68:71], v249 offset:64
	ds_read_b128 v[78:81], v249 offset:256
	ds_read_b128 v[82:85], v249 offset:320
	ds_read_b128 v[86:89], v249 offset:512
	ds_read_b128 v[90:93], v249 offset:576
	global_load_dword v8, v[168:169], off sc1
	s_waitcnt lgkmcnt(5)
	v_mfma_f32_16x16x32_f16 a[0:3], v[64:67], a[8:11], 0
	s_waitcnt lgkmcnt(4)
	v_mfma_f32_16x16x32_f16 a[0:3], v[68:71], a[12:15], a[0:3]
	s_waitcnt lgkmcnt(3)
	v_mfma_f32_16x16x32_f16 a[0:3], v[78:81], a[24:27], a[0:3]
	s_waitcnt lgkmcnt(2)
	v_mfma_f32_16x16x32_f16 a[0:3], v[82:85], a[28:31], a[0:3]
	s_waitcnt lgkmcnt(1)
	v_mfma_f32_16x16x32_f16 a[0:3], v[86:89], a[40:43], a[0:3]
	s_waitcnt lgkmcnt(0)
	v_mfma_f32_16x16x32_f16 a[4:7], v[90:93], a[44:47], a[0:3]
	v_mfma_f32_16x16x32_f16 a[0:3], v[64:67], a[16:19], 0
	v_mfma_f32_16x16x32_f16 a[0:3], v[68:71], a[20:23], a[0:3]
	v_mfma_f32_16x16x32_f16 a[0:3], v[78:81], a[32:35], a[0:3]
	v_mfma_f32_16x16x32_f16 a[0:3], v[82:85], a[36:39], a[0:3]
	v_mfma_f32_16x16x32_f16 a[0:3], v[86:89], a[48:51], a[0:3]
	v_mfma_f32_16x16x32_f16 a[0:3], v[90:93], a[52:55], a[0:3]
	global_load_dword v9, v[168:169], off sc1
.Lpl0_loop:
	s_waitcnt vmcnt(3)
	v_cmp_le_u32_e64 s[66:67], s71, v6
	s_cmp_eq_u64 s[66:67], exec
	s_cbranch_scc1 .Lpl0_done
	global_load_dword v6, v[168:169], off sc1
	s_waitcnt vmcnt(3)
	v_cmp_le_u32_e64 s[66:67], s71, v7
	s_cmp_eq_u64 s[66:67], exec
	s_cbranch_scc1 .Lpl0_done
	global_load_dword v7, v[168:169], off sc1
	s_waitcnt vmcnt(3)
	v_cmp_le_u32_e64 s[66:67], s71, v8
	s_cmp_eq_u64 s[66:67], exec
	s_cbranch_scc1 .Lpl0_done
	global_load_dword v8, v[168:169], off sc1
	s_waitcnt vmcnt(3)
	v_cmp_le_u32_e64 s[66:67], s71, v9
	s_cmp_eq_u64 s[66:67], exec
	s_cbranch_scc1 .Lpl0_done
	global_load_dword v9, v[168:169], off sc1
	s_add_i32 s65, s65, 1
	s_cmp_gt_u32 s65, 0xffff
	s_cbranch_scc0 .Lpl0_loop

.Ltg0_entry:
	v_mov_b32_e32 v250, 0
	s_waitcnt vmcnt(20) lgkmcnt(14)
	v_or3_b32 v250, v250, v55, v57
	v_mfma_f32_16x16x32_f16 a[128:131], v[54:57], v[64:67], 0
	s_waitcnt vmcnt(19)
	v_or3_b32 v250, v250, v51, v53
	v_mfma_f32_16x16x32_f16 a[128:131], v[50:53], v[78:81], a[128:131]
	v_mfma_f32_16x16x32_f16 a[132:135], v[54:57], v[68:71], 0
	s_waitcnt vmcnt(18)
	v_or3_b32 v250, v250, v47, v49
	v_mfma_f32_16x16x32_f16 a[128:131], v[46:49], v[86:89], a[128:131]
	v_mfma_f32_16x16x32_f16 a[132:135], v[50:53], v[82:85], a[132:135]
	s_waitcnt vmcnt(17)
	v_or3_b32 v250, v250, v43, v45
	v_mfma_f32_16x16x32_f16 a[128:131], v[42:45], v[94:97], a[128:131]
	v_mfma_f32_16x16x32_f16 a[132:135], v[46:49], v[90:93], a[132:135]
	s_waitcnt vmcnt(16)
	v_or3_b32 v250, v250, v39, v41
	v_mfma_f32_16x16x32_f16 a[128:131], v[38:41], v[190:193], a[128:131]
	v_mfma_f32_16x16x32_f16 a[132:135], v[42:45], v[98:101], a[132:135]
	s_waitcnt vmcnt(15)
	v_or3_b32 v250, v250, v35, v37
	v_mfma_f32_16x16x32_f16 a[128:131], v[34:37], v[106:109], a[128:131]
	v_mfma_f32_16x16x32_f16 a[132:135], v[38:41], v[102:105], a[132:135]
	s_waitcnt vmcnt(14) lgkmcnt(13)
	v_or3_b32 v250, v250, v31, v33
	v_mfma_f32_16x16x32_f16 a[128:131], v[30:33], v[118:121], a[128:131]
	v_mfma_f32_16x16x32_f16 a[132:135], v[34:37], v[114:117], a[132:135]
	s_waitcnt vmcnt(13) lgkmcnt(11)
	v_or3_b32 v250, v250, v27, v29
	v_mfma_f32_16x16x32_f16 a[128:131], v[26:29], v[126:129], a[128:131]
	v_mfma_f32_16x16x32_f16 a[132:135], v[30:33], v[122:125], a[132:135]
	s_waitcnt vmcnt(12) lgkmcnt(9)
	v_or3_b32 v250, v250, v23, v25
	v_mfma_f32_16x16x32_f16 a[128:131], v[22:25], v[134:137], a[128:131]
	v_mfma_f32_16x16x32_f16 a[132:135], v[26:29], v[130:133], a[132:135]
	s_waitcnt vmcnt(11) lgkmcnt(7)
	v_or3_b32 v250, v250, v19, v21
	v_mfma_f32_16x16x32_f16 a[128:131], v[18:21], v[142:145], a[128:131]
	v_mfma_f32_16x16x32_f16 a[132:135], v[22:25], v[138:141], a[132:135]
	s_waitcnt vmcnt(10) lgkmcnt(5)
	v_or3_b32 v250, v250, v15, v17
	v_mfma_f32_16x16x32_f16 a[128:131], v[14:17], v[150:153], a[128:131]
	v_mfma_f32_16x16x32_f16 a[132:135], v[18:21], v[146:149], a[132:135]
	s_waitcnt vmcnt(9) lgkmcnt(3)
	v_or3_b32 v250, v250, v11, v13
	v_mfma_f32_16x16x32_f16 a[128:131], v[10:13], v[158:161], a[128:131]
	v_mfma_f32_16x16x32_f16 a[132:135], v[14:17], v[154:157], a[132:135]
	s_waitcnt vmcnt(8) lgkmcnt(0)
	v_or3_b32 v250, v250, v7, v9
	v_mfma_f32_16x16x32_f16 a[128:131], v[6:9], v[72:75], a[128:131]
	v_mfma_f32_16x16x32_f16 a[132:135], v[10:13], v[162:165], a[132:135]
	v_mfma_f32_16x16x32_f16 a[132:135], v[6:9], v[0:3], a[132:135]
	v_and_b32_e32 v250, s64, v250
	v_cmp_ne_u32_e64 s[66:67], 0, v250
	s_cmp_lg_u64 s[66:67], 0
	s_cbranch_scc1 .Ltg0_redo
.Ltg0_go:
	s_nop 1
	v_accvgpr_read_b32 v10, a128
	v_accvgpr_read_b32 v11, a129
	v_accvgpr_read_b32 v12, a130
	v_accvgpr_read_b32 v13, a131
	v_cvt_pk_f16_f32 v1, v12, v13
	v_cvt_pk_f16_f32 v0, v10, v11
	v_accvgpr_read_b32 v6, a132
	v_accvgpr_read_b32 v7, a133
	v_accvgpr_read_b32 v8, a134
	v_accvgpr_read_b32 v9, a135
	v_cvt_pk_f16_f32 v3, v8, v9
	v_cvt_pk_f16_f32 v2, v6, v7
	ds_write2_b64 v221, v[0:1], v[2:3] offset0:48 offset1:80
	s_cbranch_vccnz .LBB1_93
	s_and_saveexec_b64 s[36:37], s[6:7]
	s_cbranch_execz .LBB1_92
	v_add_u32_e32 v0, 0x8400, v60
	s_waitcnt vmcnt(0)
	ds_write2_b32 v0, v181, v184 offset1:16
	ds_write_b32 v60, v185 offset:33920

.LBB1_109:
	v_accvgpr_read_b32 v0, a0
	v_accvgpr_read_b32 v1, a1
	v_accvgpr_read_b32 v2, a2
	v_accvgpr_read_b32 v3, a3
	v_fma_mixlo_f16 v18, v20, v24, 0
	v_fma_mixlo_f16 v19, v21, v25, 0
	v_fma_mixlo_f16 v20, v22, v26, 0
	v_fma_mixlo_f16 v21, v23, v27, 0
	v_mul_f32_e32 v10, v255, v10
	v_fmac_f32_e32 v10, v254, v6
	v_add_f32_e32 v0, v252, v0
	v_fmac_f32_e32 v10, v253, v14
	v_add_f32_e32 v0, v0, v10
	v_mul_f32_e32 v0, 0xbfb8aa3b, v0
	v_exp_f32_e32 v0, v0
	v_mul_f32_e32 v6, v255, v11
	v_fmac_f32_e32 v6, v254, v7
	v_add_f32_e32 v1, v252, v1
	v_fmac_f32_e32 v6, v253, v15
	v_add_f32_e32 v1, v1, v6
	v_add_f32_e32 v0, 1.0, v0
	v_mul_f32_e32 v1, 0xbfb8aa3b, v1
	v_rcp_f32_e32 v0, v0
	v_exp_f32_e32 v1, v1
	ds_write_b32 v184, v0 offset:29696
	ds_write_b16 v247, v18 offset:12800
	v_add_f32_e32 v0, 1.0, v1
	v_add_f32_e32 v1, v252, v2
	v_mul_f32_e32 v2, v255, v12
	v_fmac_f32_e32 v2, v254, v8
	v_fmac_f32_e32 v2, v253, v16
	v_add_f32_e32 v1, v1, v2
	v_add_f32_e32 v2, v252, v3
	v_mul_f32_e32 v3, v255, v13
	v_fmac_f32_e32 v3, v254, v9
	v_mul_f32_e32 v1, 0xbfb8aa3b, v1
	v_fmac_f32_e32 v3, v253, v17
	v_rcp_f32_e32 v0, v0
	v_exp_f32_e32 v1, v1
	v_add_f32_e32 v2, v2, v3
	v_mul_f32_e32 v2, 0xbfb8aa3b, v2
	v_exp_f32_e32 v2, v2
	ds_write_b32 v250, v0 offset:29696
	v_add_f32_e32 v0, 1.0, v1
	v_rcp_f32_e32 v0, v0
	v_add_f32_e32 v1, 1.0, v2
	v_rcp_f32_e32 v1, v1
	ds_write_b16 v247, v19 offset:13344
	ds_write_b32 v185, v0 offset:29696
	ds_write_b16 v247, v20 offset:13888
	ds_write_b32 v251, v1 offset:29696
	ds_write_b16 v247, v21 offset:14432
	s_xor_b64 s[30:31], s[30:31], -1
	s_andn2_b64 vcc, exec, s[30:31]
	s_mov_b64 s[30:31], -1
	s_add_i32 s71, s40, 1
	global_load_dword v50, v[168:169], off sc1
	global_load_dword v51, v[168:169], off sc1
	ds_read_b128 v[54:57], v208 offset:34832
	ds_read_b128 v[64:67], v208 offset:48144
	ds_read_b128 v[68:71], v209 offset:34832
	ds_read_b128 v[72:75], v209 offset:48144
	ds_read_b128 v[78:81], v210 offset:34832
	ds_read_b128 v[82:85], v210 offset:48144
	ds_read_b128 v[86:89], v211 offset:34832
	ds_read_b128 v[90:93], v211 offset:48144
	ds_read_b128 v[94:97], v212 offset:34832
	ds_read_b128 v[98:101], v212 offset:48144
	ds_read_b128 v[102:105], v213 offset:34832
	ds_read_b128 v[106:109], v213 offset:48144
	ds_read_b128 v[114:117], v214 offset:34832
	global_load_dword v52, v[168:169], off sc1
	ds_read_b128 v[118:121], v214 offset:48144
	ds_read_b128 v[122:125], v215 offset:34832
	ds_read_b128 v[126:129], v215 offset:48144
	ds_read_b128 v[130:133], v216 offset:34832
	ds_read_b128 v[134:137], v216 offset:48144
	ds_read_b128 v[138:141], v217 offset:34832
	ds_read_b128 v[142:145], v217 offset:48144
	ds_read_b128 v[146:149], v218 offset:34832
	ds_read_b128 v[150:153], v218 offset:48144
	ds_read_b128 v[154:157], v219 offset:34832
	ds_read_b128 v[158:161], v219 offset:48144
	ds_read_b128 v[162:165], v220 offset:34832
	ds_read_b128 v[180:183], v220 offset:48144
	global_load_dword v53, v[168:169], off sc1
.Lpl1_loop:
	s_waitcnt vmcnt(3)
	v_cmp_le_u32_e64 s[66:67], s71, v50
	s_cmp_eq_u64 s[66:67], exec
	s_cbranch_scc1 .Lpl1_done
	global_load_dword v50, v[168:169], off sc1
	s_waitcnt vmcnt(3)
	v_cmp_le_u32_e64 s[66:67], s71, v51
	s_cmp_eq_u64 s[66:67], exec
	s_cbranch_scc1 .Lpl1_done
	global_load_dword v51, v[168:169], off sc1
	s_waitcnt vmcnt(3)
	v_cmp_le_u32_e64 s[66:67], s71, v52
	s_cmp_eq_u64 s[66:67], exec
	s_cbranch_scc1 .Lpl1_done
	global_load_dword v52, v[168:169], off sc1
	s_waitcnt vmcnt(3)
	v_cmp_le_u32_e64 s[66:67], s71, v53
	s_cmp_eq_u64 s[66:67], exec
	s_cbranch_scc1 .Lpl1_done
	global_load_dword v53, v[168:169], off sc1
	s_add_i32 s65, s65, 1
	s_cmp_gt_u32 s65, 0xffff
	s_cbranch_scc0 .Lpl1_loop

.Ltg1_entry:
	v_mov_b32_e32 v255, 0
	s_waitcnt vmcnt(16) lgkmcnt(14)
	v_xor_b32_e32 v1, s64, v1
	v_xor_b32_e32 v3, s64, v3
	v_or3_b32 v255, v255, v1, v3
	s_nop 0
	v_mfma_f32_16x16x32_f16 a[0:3], v[0:3], v[54:57], 0
	v_mfma_f32_16x16x32_f16 a[4:7], v[0:3], v[64:67], 0
	s_waitcnt vmcnt(15)
	v_xor_b32_e32 v7, s64, v7
	v_xor_b32_e32 v9, s64, v9
	v_or3_b32 v255, v255, v7, v9
	s_nop 0
	v_mfma_f32_16x16x32_f16 a[0:3], v[6:9], v[68:71], a[0:3]
	v_mfma_f32_16x16x32_f16 a[4:7], v[6:9], v[72:75], a[4:7]
	s_waitcnt vmcnt(14)
	v_xor_b32_e32 v11, s64, v11
	v_xor_b32_e32 v13, s64, v13
	v_or3_b32 v255, v255, v11, v13
	s_nop 0
	v_mfma_f32_16x16x32_f16 a[0:3], v[10:13], v[78:81], a[0:3]
	v_mfma_f32_16x16x32_f16 a[4:7], v[10:13], v[82:85], a[4:7]
	s_waitcnt vmcnt(13)
	v_xor_b32_e32 v15, s64, v15
	v_xor_b32_e32 v17, s64, v17
	v_or3_b32 v255, v255, v15, v17
	s_nop 0
	v_mfma_f32_16x16x32_f16 a[0:3], v[14:17], v[86:89], a[0:3]
	v_mfma_f32_16x16x32_f16 a[4:7], v[14:17], v[90:93], a[4:7]
	s_waitcnt vmcnt(12)
	v_xor_b32_e32 v19, s64, v19
	v_xor_b32_e32 v21, s64, v21
	v_or3_b32 v255, v255, v19, v21
	s_nop 0
	v_mfma_f32_16x16x32_f16 a[0:3], v[18:21], v[94:97], a[0:3]
	v_mfma_f32_16x16x32_f16 a[4:7], v[18:21], v[98:101], a[4:7]
	s_waitcnt vmcnt(11)
	v_xor_b32_e32 v23, s64, v23
	v_xor_b32_e32 v25, s64, v25
	v_or3_b32 v255, v255, v23, v25
	s_nop 0
	v_mfma_f32_16x16x32_f16 a[0:3], v[22:25], v[102:105], a[0:3]
	v_mfma_f32_16x16x32_f16 a[4:7], v[22:25], v[106:109], a[4:7]
	s_waitcnt vmcnt(10) lgkmcnt(13)
	v_xor_b32_e32 v27, s64, v27
	v_xor_b32_e32 v29, s64, v29
	v_or3_b32 v255, v255, v27, v29
	s_nop 0
	v_mfma_f32_16x16x32_f16 a[0:3], v[26:29], v[114:117], a[0:3]
	s_waitcnt lgkmcnt(12)
	v_mfma_f32_16x16x32_f16 a[4:7], v[26:29], v[118:121], a[4:7]
	s_waitcnt vmcnt(9) lgkmcnt(11)
	v_xor_b32_e32 v31, s64, v31
	v_xor_b32_e32 v33, s64, v33
	v_or3_b32 v255, v255, v31, v33
	s_nop 0
	v_mfma_f32_16x16x32_f16 a[0:3], v[30:33], v[122:125], a[0:3]
	s_waitcnt lgkmcnt(10)
	v_mfma_f32_16x16x32_f16 a[4:7], v[30:33], v[126:129], a[4:7]
	s_waitcnt vmcnt(8) lgkmcnt(9)
	v_xor_b32_e32 v35, s64, v35
	v_xor_b32_e32 v37, s64, v37
	v_or3_b32 v255, v255, v35, v37
	s_nop 0
	v_mfma_f32_16x16x32_f16 a[0:3], v[34:37], v[130:133], a[0:3]
	s_waitcnt lgkmcnt(8)
	v_mfma_f32_16x16x32_f16 a[4:7], v[34:37], v[134:137], a[4:7]
	s_waitcnt vmcnt(7) lgkmcnt(7)
	v_xor_b32_e32 v39, s64, v39
	v_xor_b32_e32 v41, s64, v41
	v_or3_b32 v255, v255, v39, v41
	s_nop 0
	v_mfma_f32_16x16x32_f16 a[0:3], v[38:41], v[138:141], a[0:3]
	s_waitcnt lgkmcnt(6)
	v_mfma_f32_16x16x32_f16 a[4:7], v[38:41], v[142:145], a[4:7]
	s_waitcnt vmcnt(6) lgkmcnt(5)
	v_xor_b32_e32 v43, s64, v43
	v_xor_b32_e32 v45, s64, v45
	v_or3_b32 v255, v255, v43, v45
	s_nop 0
	v_mfma_f32_16x16x32_f16 a[0:3], v[42:45], v[146:149], a[0:3]
	s_waitcnt lgkmcnt(4)
	v_mfma_f32_16x16x32_f16 a[4:7], v[42:45], v[150:153], a[4:7]
	s_waitcnt vmcnt(5) lgkmcnt(3)
	v_xor_b32_e32 v47, s64, v47
	v_xor_b32_e32 v49, s64, v49
	v_or3_b32 v255, v255, v47, v49
	s_nop 0
	v_mfma_f32_16x16x32_f16 a[0:3], v[46:49], v[154:157], a[0:3]
	s_waitcnt vmcnt(4) lgkmcnt(0)
	v_xor_b32_e32 v51, s64, v51
	v_xor_b32_e32 v53, s64, v53
	v_or3_b32 v255, v255, v51, v53
	s_nop 0
	v_mfma_f32_16x16x32_f16 a[0:3], v[50:53], v[162:165], a[0:3]
	v_mfma_f32_16x16x32_f16 a[4:7], v[46:49], v[158:161], a[4:7]
	v_mfma_f32_16x16x32_f16 a[4:7], v[50:53], v[180:183], a[4:7]
	v_and_b32_e32 v255, s64, v255
	v_cmp_ne_u32_e64 s[66:67], 0, v255
	s_cmp_lg_u64 s[66:67], 0
	s_cbranch_scc1 .Ltg1_redo
.Ltg1_go:
	s_nop 1
	v_accvgpr_read_b32 v0, a0
	v_accvgpr_read_b32 v2, a1
	v_accvgpr_read_b32 v1, a2
	v_accvgpr_read_b32 v3, a3
	v_cvt_pk_f16_f32 v1, v1, v3
	v_cvt_pk_f16_f32 v0, v0, v2
	v_add_u32_e32 v182, v111, v207
	v_accvgpr_read_b32 v2, a4
	v_accvgpr_read_b32 v6, a5
	v_accvgpr_read_b32 v3, a6
	v_accvgpr_read_b32 v7, a7
	v_cvt_pk_f16_f32 v3, v3, v7
	v_cvt_pk_f16_f32 v2, v2, v6
	ds_write2_b64 v248, v[0:1], v[2:3] offset0:80 offset1:96
	s_waitcnt lgkmcnt(0)
	s_barrier
	ds_read_b128 v[0:3], v182 offset:12800
	ds_read_b128 v[6:9], v182 offset:12864
	ds_read_b128 v[10:13], v182 offset:12928
	ds_read_b128 v[14:17], v182 offset:12992
	ds_read_b128 v[18:21], v182 offset:13056
	ds_read_b128 v[22:25], v182 offset:13120
	ds_read2st64_b32 v[42:43], v242 offset0:84 offset1:116
	ds_read_b128 v[38:41], v225 offset:33792
	ds_read_b128 v[26:29], v225 offset:33856
	ds_read_b128 v[30:33], v225 offset:33920
	v_or_b32_e32 v36, v110, v227
	v_or_b32_e32 v34, v110, v226
	ds_read2st64_b32 v[44:45], v36 offset0:84 offset1:116
	v_or_b32_e32 v36, v110, v228
	ds_read2st64_b32 v[34:35], v34 offset0:84 offset1:116
	ds_read2st64_b32 v[36:37], v36 offset0:84 offset1:116
	s_waitcnt lgkmcnt(12)
	v_mfma_f32_16x16x32_f16 a[0:3], v[0:3], a[56:59], 0
	s_waitcnt lgkmcnt(11)
	v_mfma_f32_16x16x32_f16 a[0:3], v[6:9], a[60:63], a[0:3]
	s_waitcnt lgkmcnt(10)
	v_mfma_f32_16x16x32_f16 a[0:3], v[10:13], a[64:67], a[0:3]
	s_waitcnt lgkmcnt(9)
	v_mfma_f32_16x16x32_f16 a[0:3], v[14:17], a[68:71], a[0:3]
	s_waitcnt lgkmcnt(8)
	v_mfma_f32_16x16x32_f16 a[0:3], v[18:21], a[72:75], a[0:3]
	s_waitcnt lgkmcnt(7)
	v_mfma_f32_16x16x32_f16 a[0:3], v[22:25], a[76:79], a[0:3]
	s_nop 7
	v_accvgpr_read_b32 v7, a1
	v_accvgpr_read_b32 v9, a0
	v_accvgpr_read_b32 v1, a3
	v_accvgpr_read_b32 v3, a2
	s_waitcnt lgkmcnt(5)
	v_mov_b32_e32 v10, v38
	s_waitcnt lgkmcnt(4)
	v_mov_b32_e32 v11, v26
	s_waitcnt vmcnt(1)
	v_mul_f32_e32 v0, v191, v26
	v_pk_fma_f32 v[10:11], v[190:191], v[10:11], v[0:1] op_sel_hi:[1,1,0]
	s_waitcnt vmcnt(0) lgkmcnt(3)
	v_mul_f32_e32 v8, v192, v30
	v_mov_b32_e32 v11, v186
	v_pk_add_f32 v[8:9], v[10:11], v[8:9]
	v_mov_b32_e32 v26, v39
	v_add_f32_e32 v0, v8, v9
	v_mul_f32_e32 v0, 0x4038aa3b, v0
	v_exp_f32_e32 v2, v0
	v_mul_f32_e32 v0, v191, v27
	v_pk_fma_f32 v[8:9], v[190:191], v[26:27], v[0:1] op_sel_hi:[1,1,0]
	v_mul_f32_e32 v6, v192, v31
	v_mov_b32_e32 v9, v186
	v_pk_add_f32 v[6:7], v[8:9], v[6:7]
	v_mov_b32_e32 v10, v40
	v_add_f32_e32 v0, v6, v7
	v_mul_f32_e32 v0, 0x4038aa3b, v0
	v_exp_f32_e32 v0, v0
	v_mov_b32_e32 v11, v28
	v_add_f32_e32 v2, 1.0, v2
	v_rcp_f32_e32 v6, v2
	v_add_f32_e32 v0, 1.0, v0
	v_rcp_f32_e32 v7, v0
	v_mul_f32_e32 v0, v191, v28
	v_pk_fma_f32 v[10:11], v[190:191], v[10:11], v[0:1] op_sel_hi:[1,1,0]
	v_mul_f32_e32 v2, v192, v32
	v_mov_b32_e32 v11, v186
	v_pk_add_f32 v[2:3], v[10:11], v[2:3]
	v_mov_b32_e32 v28, v41
	v_add_f32_e32 v0, v2, v3
	v_mul_f32_e32 v2, v191, v29
	v_mul_f32_e32 v0, 0x4038aa3b, v0
	v_pk_fma_f32 v[2:3], v[190:191], v[28:29], v[2:3] op_sel_hi:[1,1,0]
	v_exp_f32_e32 v10, v0
	v_mul_f32_e32 v0, v192, v33
	v_mov_b32_e32 v3, v186
	v_pk_add_f32 v[0:1], v[2:3], v[0:1]
	v_add_f32_e32 v2, 1.0, v10
	v_add_f32_e32 v0, v0, v1
	v_mul_f32_e32 v0, 0x4038aa3b, v0
	v_exp_f32_e32 v3, v0
	v_rcp_f32_e32 v2, v2
	s_waitcnt lgkmcnt(1)
	v_mov_b32_e32 v9, v34
	v_mov_b32_e32 v34, v43
	v_add_f32_e32 v3, 1.0, v3
	v_rcp_f32_e32 v3, v3
	v_pk_fma_f32 v[6:7], v[6:7], 2.0, 1.0 op_sel_hi:[1,0,0] neg_lo:[1,0,0] neg_hi:[1,0,0]
	v_pk_add_f32 v[0:1], v[34:35], 1.0 op_sel_hi:[1,0] neg_lo:[1,0] neg_hi:[1,0]
	v_mov_b32_e32 v8, v42
	v_pk_mul_f32 v[0:1], v[0:1], v[6:7]
	s_and_b64 vcc, exec, s[16:17]
	v_pk_fma_f32 v[8:9], v[8:9], v[34:35], v[0:1]
	v_pk_fma_f32 v[0:1], v[2:3], 2.0, 1.0 op_sel_hi:[1,0,0] neg_lo:[1,0,0] neg_hi:[1,0,0]
	s_waitcnt lgkmcnt(0)
	v_mov_b32_e32 v3, v36
	v_mov_b32_e32 v36, v45
	v_pk_add_f32 v[10:11], v[36:37], 1.0 op_sel_hi:[1,0] neg_lo:[1,0] neg_hi:[1,0]
	v_mov_b32_e32 v2, v44
	v_pk_mul_f32 v[0:1], v[10:11], v[0:1]
	v_cvt_pk_f16_f32 v6, v8, v9
	v_pk_fma_f32 v[10:11], v[2:3], v[36:37], v[0:1]
	s_nop 0
	v_cvt_pk_f16_f32 v7, v10, v11
	v_mov_b32_e32 v2, v6
	v_or_b32_e32 v3, s64, v7
	s_cbranch_vccnz .LBB1_125
	s_mov_b64 s[36:37], 0
	global_store_dwordx2 v[178:179], v[2:3], off
	s_or_b32 s70, s40, 2
	s_and_saveexec_b64 s[68:69], s[12:13]
	v_mov_b32_e32 v0, s70
	global_store_dword v[174:175], v0, off
	s_mov_b64 exec, s[68:69]

.LBB1_127:
	s_or_b32 s26, s40, 2
	ds_write_b32 v184, v8 offset:21504
	ds_write_b16 v245, v6
	ds_write_b32 v250, v9 offset:21504
	ds_write_b16_d16_hi v245, v6 offset:800
	ds_write_b32 v185, v10 offset:21504
	ds_write_b16 v245, v7 offset:1600
	ds_write_b32 v251, v11 offset:21504
	ds_write_b16_d16_hi v245, v7 offset:2400
	s_xor_b64 s[30:31], s[30:31], -1
	s_andn2_b64 vcc, exec, s[30:31]
	s_mov_b64 s[30:31], -1
	s_add_i32 s71, s40, 2
	global_load_dword v50, v[168:169], off sc1
	global_load_dword v51, v[168:169], off sc1
	ds_read_b128 v[54:57], v58 offset:4096
	ds_read_b128 v[64:67], v58 offset:5120
	ds_read_b128 v[68:71], v249 offset:128
	ds_read_b128 v[72:75], v249 offset:192
	ds_read_b128 v[78:81], v58 offset:6144
	ds_read_b128 v[82:85], v58 offset:7168
	ds_read_b128 v[86:89], v58 offset:12288
	ds_read_b128 v[90:93], v58 offset:13312
	ds_read_b128 v[94:97], v249 offset:384
	ds_read_b128 v[98:101], v249 offset:448
	ds_read_b128 v[102:105], v58 offset:14336
	ds_read_b128 v[106:109], v58 offset:15360
	ds_read_b128 v[114:117], v58 offset:20480
	ds_read_b128 v[118:121], v58 offset:21504
	ds_read_b128 v[122:125], v249 offset:640
	ds_read_b128 v[126:129], v249 offset:704
	ds_read_b128 v[130:133], v58 offset:22528
	ds_read_b128 v[134:137], v58 offset:23552
	global_load_dword v52, v[168:169], off sc1
	s_waitcnt lgkmcnt(14)
	v_mfma_f32_16x16x32_f16 a[0:3], v[68:71], v[54:57], 0
	s_waitcnt lgkmcnt(13)
	v_mfma_f32_16x16x32_f16 a[0:3], v[72:75], v[78:81], a[0:3]
	s_waitcnt lgkmcnt(9)
	v_mfma_f32_16x16x32_f16 a[0:3], v[94:97], v[86:89], a[0:3]
	s_waitcnt lgkmcnt(7)
	v_mfma_f32_16x16x32_f16 a[0:3], v[98:101], v[102:105], a[0:3]
	s_waitcnt lgkmcnt(3)
	v_mfma_f32_16x16x32_f16 a[0:3], v[122:125], v[114:117], a[0:3]
	s_waitcnt lgkmcnt(1)
	v_mfma_f32_16x16x32_f16 a[4:7], v[126:129], v[130:133], a[0:3]
	v_mfma_f32_16x16x32_f16 a[0:3], v[68:71], v[64:67], 0
	v_mfma_f32_16x16x32_f16 a[0:3], v[72:75], v[82:85], a[0:3]
	v_mfma_f32_16x16x32_f16 a[0:3], v[94:97], v[90:93], a[0:3]
	v_mfma_f32_16x16x32_f16 a[0:3], v[98:101], v[106:109], a[0:3]
	v_mfma_f32_16x16x32_f16 a[0:3], v[122:125], v[118:121], a[0:3]
	s_waitcnt lgkmcnt(0)
	v_mfma_f32_16x16x32_f16 a[0:3], v[126:129], v[134:137], a[0:3]
	global_load_dword v53, v[168:169], off sc1

.Ltg2_entry:
	v_mov_b32_e32 v255, 0
	s_waitcnt vmcnt(14) lgkmcnt(14)
	v_xor_b32_e32 v1, s64, v1
	v_xor_b32_e32 v3, s64, v3
	v_or3_b32 v255, v255, v1, v3
	s_nop 0
	v_mfma_f32_16x16x32_f16 a[128:131], v[0:3], v[54:57], 0
	v_mfma_f32_16x16x32_f16 a[132:135], v[0:3], v[64:67], 0
	s_waitcnt vmcnt(13)
	v_xor_b32_e32 v7, s64, v7
	v_xor_b32_e32 v9, s64, v9
	v_or3_b32 v255, v255, v7, v9
	s_nop 0
	v_mfma_f32_16x16x32_f16 a[128:131], v[6:9], v[68:71], a[128:131]
	v_mfma_f32_16x16x32_f16 a[132:135], v[6:9], v[72:75], a[132:135]
	s_waitcnt vmcnt(12)
	v_xor_b32_e32 v11, s64, v11
	v_xor_b32_e32 v13, s64, v13
	v_or3_b32 v255, v255, v11, v13
	s_nop 0
	v_mfma_f32_16x16x32_f16 a[128:131], v[10:13], v[78:81], a[128:131]
	v_mfma_f32_16x16x32_f16 a[132:135], v[10:13], v[82:85], a[132:135]
	s_waitcnt vmcnt(11)
	v_xor_b32_e32 v15, s64, v15
	v_xor_b32_e32 v17, s64, v17
	v_or3_b32 v255, v255, v15, v17
	s_nop 0
	v_mfma_f32_16x16x32_f16 a[128:131], v[14:17], v[86:89], a[128:131]
	v_mfma_f32_16x16x32_f16 a[132:135], v[14:17], v[90:93], a[132:135]
	ds_read_b128 v[0:3], v187 offset:61456
	ds_read_b128 v[10:13], v187 offset:62480
	ds_read_b128 v[64:67], v187 offset:63504
	ds_read_b128 v[14:17], v187 offset:64528
	s_waitcnt vmcnt(10)
	v_xor_b32_e32 v19, s64, v19
	v_xor_b32_e32 v21, s64, v21
	v_or3_b32 v255, v255, v19, v21
	s_nop 0
	v_mfma_f32_16x16x32_f16 a[128:131], v[18:21], v[94:97], a[128:131]
	v_mfma_f32_16x16x32_f16 a[132:135], v[18:21], v[98:101], a[132:135]
	s_waitcnt vmcnt(9)
	v_xor_b32_e32 v23, s64, v23
	v_xor_b32_e32 v25, s64, v25
	v_or3_b32 v255, v255, v23, v25
	s_nop 0
	v_mfma_f32_16x16x32_f16 a[128:131], v[22:25], v[102:105], a[128:131]
	v_mfma_f32_16x16x32_f16 a[132:135], v[22:25], v[106:109], a[132:135]
	ds_read_b128 v[68:71], v188 offset:8192
	ds_read_b128 v[18:21], v188 offset:9216
	ds_read_b128 v[72:75], v188 offset:10240
	ds_read_b128 v[22:25], v188 offset:11264
	s_waitcnt vmcnt(8) lgkmcnt(14)
	v_xor_b32_e32 v27, s64, v27
	v_xor_b32_e32 v29, s64, v29
	v_or3_b32 v255, v255, v27, v29
	s_nop 0
	v_mfma_f32_16x16x32_f16 a[128:131], v[26:29], v[114:117], a[128:131]
	v_mfma_f32_16x16x32_f16 a[132:135], v[26:29], v[118:121], a[132:135]
	ds_read_b128 v[78:81], v188 offset:16384
	ds_read_b128 v[26:29], v188 offset:17408
	ds_read_b128 v[82:85], v188 offset:18432
	ds_read_b128 v[6:9], v188 offset:19456
	s_waitcnt vmcnt(7)
	v_xor_b32_e32 v31, s64, v31
	v_xor_b32_e32 v33, s64, v33
	v_or3_b32 v255, v255, v31, v33
	s_nop 0
	v_mfma_f32_16x16x32_f16 a[128:131], v[30:33], v[122:125], a[128:131]
	v_mfma_f32_16x16x32_f16 a[132:135], v[30:33], v[126:129], a[132:135]
	s_waitcnt vmcnt(6)
	v_xor_b32_e32 v35, s64, v35
	v_xor_b32_e32 v37, s64, v37
	v_or3_b32 v255, v255, v35, v37
	s_nop 0
	v_mfma_f32_16x16x32_f16 a[128:131], v[34:37], v[130:133], a[128:131]
	v_mfma_f32_16x16x32_f16 a[132:135], v[34:37], v[134:137], a[132:135]
	s_waitcnt vmcnt(5)
	v_xor_b32_e32 v39, s64, v39
	v_xor_b32_e32 v41, s64, v41
	v_or3_b32 v255, v255, v39, v41
	s_nop 0
	v_mfma_f32_16x16x32_f16 a[128:131], v[38:41], v[138:141], a[128:131]
	v_mfma_f32_16x16x32_f16 a[132:135], v[38:41], v[142:145], a[132:135]
	s_waitcnt vmcnt(4) lgkmcnt(14)
	v_xor_b32_e32 v43, s64, v43
	v_xor_b32_e32 v45, s64, v45
	v_or3_b32 v255, v255, v43, v45
	s_nop 0
	v_mfma_f32_16x16x32_f16 a[128:131], v[42:45], v[146:149], a[128:131]
	v_mfma_f32_16x16x32_f16 a[132:135], v[42:45], v[150:153], a[132:135]
	s_waitcnt vmcnt(3)
	v_xor_b32_e32 v47, s64, v47
	v_xor_b32_e32 v49, s64, v49
	v_or3_b32 v255, v255, v47, v49
	s_nop 0
	v_mfma_f32_16x16x32_f16 a[128:131], v[46:49], v[154:157], a[128:131]
	s_waitcnt vmcnt(2) lgkmcnt(12)
	v_xor_b32_e32 v51, s64, v51
	v_xor_b32_e32 v53, s64, v53
	v_or3_b32 v255, v255, v51, v53
	s_nop 0
	v_mfma_f32_16x16x32_f16 a[128:131], v[50:53], v[162:165], a[128:131]
	v_mfma_f32_16x16x32_f16 a[132:135], v[46:49], v[158:161], a[132:135]
	v_mfma_f32_16x16x32_f16 a[132:135], v[50:53], v[190:193], a[132:135]
	v_and_b32_e32 v255, s64, v255
	v_cmp_ne_u32_e64 s[66:67], 0, v255
	s_cmp_lg_u64 s[66:67], 0
	s_cbranch_scc1 .Ltg2_redo
.Ltg2_go:
	s_nop 1
	v_accvgpr_read_b32 v30, a128
	v_accvgpr_read_b32 v32, a129
	v_accvgpr_read_b32 v31, a130
	v_accvgpr_read_b32 v33, a131
	v_cvt_pk_f16_f32 v31, v31, v33
	v_cvt_pk_f16_f32 v30, v30, v32
	v_accvgpr_read_b32 v32, a132
	v_accvgpr_read_b32 v34, a133
	v_accvgpr_read_b32 v33, a134
	v_accvgpr_read_b32 v35, a135
	v_cvt_pk_f16_f32 v33, v33, v35
	v_cvt_pk_f16_f32 v32, v32, v34
	ds_write2_b64 v221, v[30:31], v[32:33] offset0:32 offset1:64
	s_waitcnt lgkmcnt(0)
	s_barrier
	ds_read_b128 v[34:37], v249
	ds_read_b128 v[38:41], v249 offset:64
	ds_read_b128 v[42:45], v249 offset:256
	ds_read_b128 v[46:49], v249 offset:320
	ds_read_b128 v[50:53], v249 offset:512
	ds_read_b128 v[30:33], v249 offset:576
	ds_read2st64_b32 v[56:57], v184 offset0:100 offset1:101
	ds_read2st64_b32 v[54:55], v184 offset0:102 offset1:103
	s_waitcnt lgkmcnt(7)
	v_mfma_f32_16x16x32_f16 a[4:7], v[34:37], v[0:3], a[4:7]
	s_waitcnt lgkmcnt(6)
	v_mfma_f32_16x16x32_f16 a[4:7], v[38:41], v[64:67], a[4:7]
	s_waitcnt lgkmcnt(5)
	v_mfma_f32_16x16x32_f16 a[4:7], v[42:45], v[68:71], a[4:7]
	s_waitcnt lgkmcnt(4)
	v_mfma_f32_16x16x32_f16 a[4:7], v[46:49], v[72:75], a[4:7]
	s_waitcnt lgkmcnt(3)
	v_mfma_f32_16x16x32_f16 a[4:7], v[50:53], v[78:81], a[4:7]
	s_waitcnt lgkmcnt(2)
	v_mfma_f32_16x16x32_f16 a[4:7], v[30:33], v[82:85], a[4:7]
	s_nop 7
	v_accvgpr_read_b32 v0, a4
	s_waitcnt vmcnt(0)
	v_add_f32_e32 v0, v180, v0
	v_accvgpr_read_b32 v1, a5
	v_mul_f32_e32 v0, 0xbfb8aa3b, v0
	v_add_f32_e32 v1, v180, v1
	v_exp_f32_e32 v0, v0
	v_mul_f32_e32 v1, 0xbfb8aa3b, v1
	v_exp_f32_e32 v1, v1
	v_accvgpr_read_b32 v2, a7
	v_add_f32_e32 v0, 1.0, v0
	v_rcp_f32_e32 v186, v0
	v_add_f32_e32 v0, 1.0, v1
	v_accvgpr_read_b32 v1, a6
	v_add_f32_e32 v1, v180, v1
	v_mul_f32_e32 v1, 0xbfb8aa3b, v1
	v_add_f32_e32 v2, v180, v2
	v_exp_f32_e32 v1, v1
	v_mul_f32_e32 v2, 0xbfb8aa3b, v2
	v_exp_f32_e32 v2, v2
	v_rcp_f32_e32 v252, v0
	v_add_f32_e32 v0, 1.0, v1
	v_rcp_f32_e32 v253, v0
	v_add_f32_e32 v0, 1.0, v2
	v_rcp_f32_e32 v254, v0
	s_waitcnt lgkmcnt(1)
	v_mul_f32_e32 v0, v56, v186
	v_mul_f32_e32 v1, v57, v252
	s_waitcnt lgkmcnt(0)
	v_mul_f32_e32 v2, v54, v253
	v_mul_f32_e32 v3, v55, v254
	v_cvt_pk_f16_f32 v181, v2, v3
	s_and_b64 vcc, exec, s[16:17]
	v_cvt_pk_f16_f32 v180, v0, v1
	s_cbranch_vccnz .LBB1_143
	s_mov_b64 s[36:37], 0
	global_store_dwordx2 v[172:173], v[180:181], off
	s_or_b32 s70, s40, 3
	s_and_saveexec_b64 s[68:69], s[12:13]
	v_mov_b32_e32 v3, s70
	global_store_dword v[174:175], v3, off
	s_mov_b64 exec, s[68:69]

.LBB1_145:
	s_or_b32 s26, s40, 3
	v_fma_mixlo_f16 v0, v56, v186, 0
	v_fma_mixlo_f16 v1, v57, v252, 0
	v_fma_mixlo_f16 v2, v54, v253, 0
	v_fma_mixlo_f16 v3, v55, v254, 0
	v_mfma_f32_16x16x32_f16 a[0:3], v[34:37], v[10:13], a[0:3]
	ds_write_b16 v247, v0 offset:12800
	ds_write_b16 v247, v1 offset:13344
	ds_write_b16 v247, v2 offset:13888
	v_mfma_f32_16x16x32_f16 a[0:3], v[38:41], v[14:17], a[0:3]
	v_mfma_f32_16x16x32_f16 a[0:3], v[42:45], v[18:21], a[0:3]
	v_mfma_f32_16x16x32_f16 a[0:3], v[46:49], v[22:25], a[0:3]
	v_mfma_f32_16x16x32_f16 a[0:3], v[50:53], v[26:29], a[0:3]
	v_mfma_f32_16x16x32_f16 a[0:3], v[30:33], v[6:9], a[0:3]
	s_nop 7
	v_accvgpr_read_b32 v0, a0
	v_accvgpr_read_b32 v1, a1
	v_add_f32_e32 v0, v183, v0
	v_accvgpr_read_b32 v2, a2
	v_add_f32_e32 v1, v183, v1
	v_mul_f32_e32 v0, 0xbfb8aa3b, v0
	v_accvgpr_read_b32 v6, a3
	v_add_f32_e32 v2, v183, v2
	v_mul_f32_e32 v1, 0xbfb8aa3b, v1
	v_exp_f32_e32 v0, v0
	v_add_f32_e32 v6, v183, v6
	v_mul_f32_e32 v2, 0xbfb8aa3b, v2
	v_exp_f32_e32 v1, v1
	v_mul_f32_e32 v6, 0xbfb8aa3b, v6
	v_exp_f32_e32 v2, v2
	v_exp_f32_e32 v6, v6
	v_add_f32_e32 v0, 1.0, v0
	v_add_f32_e32 v1, 1.0, v1
	v_rcp_f32_e32 v0, v0
	v_add_f32_e32 v2, 1.0, v2
	v_rcp_f32_e32 v1, v1
	v_add_f32_e32 v6, 1.0, v6
	v_rcp_f32_e32 v2, v2
	v_rcp_f32_e32 v6, v6
	ds_write_b32 v184, v0 offset:29696
	ds_write_b32 v250, v1 offset:29696
	ds_write_b32 v185, v2 offset:29696
	ds_write_b32 v251, v6 offset:29696
	ds_write_b16 v247, v3 offset:14432
	s_xor_b64 s[30:31], s[30:31], -1
	s_andn2_b64 vcc, exec, s[30:31]
	s_mov_b64 s[30:31], -1
	s_add_i32 s71, s40, 3
	global_load_dword v50, v[168:169], off sc1
	global_load_dword v51, v[168:169], off sc1
	ds_read_b128 v[54:57], v249
	ds_read_b128 v[64:67], v249 offset:64
	ds_read_b128 v[68:71], v249 offset:256
	ds_read_b128 v[72:75], v249 offset:320
	ds_read_b128 v[78:81], v249 offset:512
	ds_read_b128 v[82:85], v249 offset:576
	global_load_dword v52, v[168:169], off sc1
	s_waitcnt lgkmcnt(5)
	v_mfma_f32_16x16x32_f16 a[0:3], v[54:57], a[80:83], 0
	s_waitcnt lgkmcnt(4)
	v_mfma_f32_16x16x32_f16 a[0:3], v[64:67], a[84:87], a[0:3]
	s_waitcnt lgkmcnt(3)
	v_mfma_f32_16x16x32_f16 a[0:3], v[68:71], a[96:99], a[0:3]
	s_waitcnt lgkmcnt(2)
	v_mfma_f32_16x16x32_f16 a[0:3], v[72:75], a[100:103], a[0:3]
	s_waitcnt lgkmcnt(1)
	v_mfma_f32_16x16x32_f16 a[0:3], v[78:81], a[112:115], a[0:3]
	s_waitcnt lgkmcnt(0)
	v_mfma_f32_16x16x32_f16 a[0:3], v[82:85], a[116:119], a[0:3]
	global_load_dword v53, v[168:169], off sc1

.Ltg3_entry:
	v_mov_b32_e32 v255, 0
	s_waitcnt vmcnt(13) lgkmcnt(14)
	v_or3_b32 v255, v255, v1, v3
	v_mfma_f32_16x16x32_f16 a[4:7], v[0:3], v[54:57], 0
	v_mfma_f32_16x16x32_f16 a[128:131], v[0:3], v[64:67], 0
	s_waitcnt vmcnt(12)
	v_or3_b32 v255, v255, v7, v9
	v_mfma_f32_16x16x32_f16 a[4:7], v[6:9], v[68:71], a[4:7]
	v_mfma_f32_16x16x32_f16 a[128:131], v[6:9], v[72:75], a[128:131]
	s_waitcnt vmcnt(11)
	v_or3_b32 v255, v255, v11, v13
	v_mfma_f32_16x16x32_f16 a[4:7], v[10:13], v[78:81], a[4:7]
	v_mfma_f32_16x16x32_f16 a[128:131], v[10:13], v[82:85], a[128:131]
	s_waitcnt vmcnt(10)
	v_or3_b32 v255, v255, v15, v17
	v_mfma_f32_16x16x32_f16 a[4:7], v[14:17], v[86:89], a[4:7]
	v_mfma_f32_16x16x32_f16 a[128:131], v[14:17], v[90:93], a[128:131]
	s_waitcnt vmcnt(9)
	v_or3_b32 v255, v255, v19, v21
	v_mfma_f32_16x16x32_f16 a[4:7], v[18:21], v[94:97], a[4:7]
	v_mfma_f32_16x16x32_f16 a[128:131], v[18:21], v[98:101], a[128:131]
	s_waitcnt vmcnt(8)
	v_or3_b32 v255, v255, v23, v25
	v_mfma_f32_16x16x32_f16 a[4:7], v[22:25], v[102:105], a[4:7]
	v_mfma_f32_16x16x32_f16 a[128:131], v[22:25], v[106:109], a[128:131]
	s_waitcnt vmcnt(7) lgkmcnt(13)
	v_or3_b32 v255, v255, v27, v29
	v_mfma_f32_16x16x32_f16 a[4:7], v[26:29], v[114:117], a[4:7]
	s_waitcnt lgkmcnt(12)
	v_mfma_f32_16x16x32_f16 a[128:131], v[26:29], v[118:121], a[128:131]
	s_waitcnt vmcnt(6) lgkmcnt(11)
	v_or3_b32 v255, v255, v31, v33
	v_mfma_f32_16x16x32_f16 a[4:7], v[30:33], v[122:125], a[4:7]
	s_waitcnt lgkmcnt(10)
	v_mfma_f32_16x16x32_f16 a[128:131], v[30:33], v[126:129], a[128:131]
	s_waitcnt vmcnt(5) lgkmcnt(9)
	v_or3_b32 v255, v255, v35, v37
	v_mfma_f32_16x16x32_f16 a[4:7], v[34:37], v[130:133], a[4:7]
	s_waitcnt lgkmcnt(8)
	v_mfma_f32_16x16x32_f16 a[128:131], v[34:37], v[134:137], a[128:131]
	s_waitcnt vmcnt(4) lgkmcnt(7)
	v_or3_b32 v255, v255, v39, v41
	v_mfma_f32_16x16x32_f16 a[4:7], v[38:41], v[138:141], a[4:7]
	s_waitcnt lgkmcnt(6)
	v_mfma_f32_16x16x32_f16 a[128:131], v[38:41], v[142:145], a[128:131]
	s_waitcnt vmcnt(3) lgkmcnt(5)
	v_or3_b32 v255, v255, v43, v45
	v_mfma_f32_16x16x32_f16 a[4:7], v[42:45], v[146:149], a[4:7]
	s_waitcnt lgkmcnt(4)
	v_mfma_f32_16x16x32_f16 a[128:131], v[42:45], v[150:153], a[128:131]
	s_waitcnt vmcnt(2) lgkmcnt(3)
	v_or3_b32 v255, v255, v47, v49
	v_mfma_f32_16x16x32_f16 a[4:7], v[46:49], v[154:157], a[4:7]
	s_waitcnt vmcnt(1) lgkmcnt(0)
	v_or3_b32 v255, v255, v51, v53
	v_mfma_f32_16x16x32_f16 a[4:7], v[50:53], v[162:165], a[4:7]
	v_mfma_f32_16x16x32_f16 a[128:131], v[46:49], v[158:161], a[128:131]
	v_mfma_f32_16x16x32_f16 a[128:131], v[50:53], v[190:193], a[128:131]
	v_and_b32_e32 v255, s64, v255
	v_cmp_ne_u32_e64 s[66:67], 0, v255
	s_cmp_lg_u64 s[66:67], 0
	s_cbranch_scc1 .Ltg3_redo
.Ltg3_go:
	s_nop 1
	v_accvgpr_read_b32 v0, a4
	v_accvgpr_read_b32 v2, a5
	v_accvgpr_read_b32 v1, a6
	v_accvgpr_read_b32 v3, a7
	v_cvt_pk_f16_f32 v1, v1, v3
	v_cvt_pk_f16_f32 v0, v0, v2
	v_accvgpr_read_b32 v2, a128
	v_accvgpr_read_b32 v6, a129
	v_accvgpr_read_b32 v3, a130
	v_accvgpr_read_b32 v7, a131
	v_cvt_pk_f16_f32 v3, v3, v7
	v_cvt_pk_f16_f32 v2, v2, v6
	ds_write2_b64 v221, v[0:1], v[2:3] offset0:48 offset1:80
	s_waitcnt lgkmcnt(0)
	s_barrier
	ds_read_b128 v[0:3], v182 offset:12800
	ds_read_b128 v[6:9], v182 offset:12864
	ds_read_b128 v[10:13], v249 offset:384
	ds_read_b128 v[14:17], v249 offset:448
	ds_read_b128 v[18:21], v249 offset:640
	ds_read_b128 v[22:25], v249 offset:704
	ds_read2st64_b32 v[26:27], v242 offset0:100 offset1:101
	ds_read2st64_b32 v[28:29], v242 offset0:116 offset1:117
	ds_read2st64_b32 v[30:31], v242 offset0:118 offset1:119
	ds_read2st64_b32 v[32:33], v242 offset0:102 offset1:103
	s_waitcnt lgkmcnt(9)
	v_mfma_f32_16x16x32_f16 a[0:3], v[0:3], a[88:91], a[0:3]
	s_waitcnt lgkmcnt(8)
	v_mfma_f32_16x16x32_f16 a[0:3], v[6:9], a[92:95], a[0:3]
	s_waitcnt lgkmcnt(7)
	v_mfma_f32_16x16x32_f16 a[0:3], v[10:13], a[104:107], a[0:3]
	s_waitcnt lgkmcnt(6)
	v_mfma_f32_16x16x32_f16 a[0:3], v[14:17], a[108:111], a[0:3]
	s_waitcnt lgkmcnt(5)
	v_mfma_f32_16x16x32_f16 a[0:3], v[18:21], a[120:123], a[0:3]
	s_waitcnt lgkmcnt(4)
	v_mfma_f32_16x16x32_f16 a[0:3], v[22:25], a[124:127], a[0:3]
	s_nop 7
	v_accvgpr_read_b32 v0, a0
	v_accvgpr_read_b32 v1, a1
	s_waitcnt vmcnt(0)
	v_add_f32_e32 v0, v180, v0
	v_add_f32_e32 v1, v180, v1
	v_mul_f32_e32 v0, 0x4038aa3b, v0
	v_mul_f32_e32 v1, 0x4038aa3b, v1
	v_exp_f32_e32 v0, v0
	v_exp_f32_e32 v1, v1
	s_waitcnt lgkmcnt(2)
	v_pk_add_f32 v[2:3], v[28:29], 1.0 op_sel_hi:[1,0] neg_lo:[1,0] neg_hi:[1,0]
	s_and_b64 vcc, exec, s[16:17]
	v_add_f32_e32 v0, 1.0, v0
	v_add_f32_e32 v1, 1.0, v1
	v_rcp_f32_e32 v0, v0
	v_rcp_f32_e32 v1, v1
	s_nop 0
	v_pk_fma_f32 v[0:1], v[0:1], 2.0, 1.0 op_sel_hi:[1,0,0] neg_lo:[1,0,0] neg_hi:[1,0,0]
	s_nop 0
	v_pk_mul_f32 v[0:1], v[2:3], v[0:1]
	s_waitcnt lgkmcnt(1)
	v_pk_add_f32 v[2:3], v[30:31], 1.0 op_sel_hi:[1,0] neg_lo:[1,0] neg_hi:[1,0]
	v_pk_fma_f32 v[6:7], v[26:27], v[28:29], v[0:1]
	v_accvgpr_read_b32 v0, a2
	v_accvgpr_read_b32 v1, a3
	v_add_f32_e32 v0, v180, v0
	v_add_f32_e32 v1, v180, v1
	v_mul_f32_e32 v0, 0x4038aa3b, v0
	v_mul_f32_e32 v1, 0x4038aa3b, v1
	v_exp_f32_e32 v0, v0
	v_exp_f32_e32 v1, v1
	v_cvt_pk_f16_f32 v10, v6, v7
	v_add_f32_e32 v0, 1.0, v0
	v_add_f32_e32 v1, 1.0, v1
	v_rcp_f32_e32 v0, v0
	v_rcp_f32_e32 v1, v1
	s_nop 0
	v_pk_fma_f32 v[0:1], v[0:1], 2.0, 1.0 op_sel_hi:[1,0,0] neg_lo:[1,0,0] neg_hi:[1,0,0]
	s_nop 0
	v_pk_mul_f32 v[0:1], v[2:3], v[0:1]
	s_waitcnt lgkmcnt(0)
	v_pk_fma_f32 v[8:9], v[32:33], v[30:31], v[0:1]
	s_nop 0
	v_cvt_pk_f16_f32 v11, v8, v9
	s_cbranch_vccnz .LBB1_172
	global_store_dwordx2 v[178:179], v[10:11], off
	s_add_i32 s70, s40, 4
	s_and_saveexec_b64 s[68:69], s[12:13]
	v_mov_b32_e32 v3, s70
	global_store_dword v[174:175], v3, off
	s_mov_b64 exec, s[68:69]
	s_cbranch_execnz .LBB1_162
